# bundle9 + attention V tile: odd rows stored 16B lower so transposed V reads and V writes are bank-conflict free
# speedup vs baseline: 1.0014x; 1.0014x over previous
.LBB0_411:
	s_or_b64 exec, exec, s[56:57]
	v_readlane_b32 s23, v254, 12
	s_mov_b32 s70, s59
	s_waitcnt lgkmcnt(0)
	s_barrier
	v_mbcnt_lo_u32_b32 v49, -1, 0
	v_mbcnt_hi_u32_b32 v49, -1, v49
	s_lshr_b32 s6, s70, 5
	s_and_b32 s7, s70, 31
	s_mulk_i32 s6, 0xc00
	s_or_b32 s24, s6, s7
	s_mul_hi_i32 s6, s24, 0x2aaaaaab
	s_lshr_b32 s8, s6, 31
	s_ashr_i32 s6, s6, 5
	s_add_i32 s8, s6, s8
	s_mul_i32 s6, s8, 0xffffff40
	s_add_i32 s6, s6, s24
	s_ashr_i32 s30, s6, 6
	s_ashr_i32 s10, s8, 4
	s_cmp_eq_u32 s30, 1
	s_cselect_b32 s9, 3, 15
	s_cselect_b32 s11, 2, 4
	s_cmp_lt_u32 s6, 64
	s_cselect_b32 s12, 0, s11
	s_cselect_b32 s6, 0, s9
	s_lshr_b32 s25, s7, s12
	v_lshl_add_u32 v50, s23, 6, v49
	v_sub_u32_e64 v0, s25, 1 clamp
	s_ashr_i32 s9, s8, 31
	v_lshlrev_b32_e32 v4, 7, v0
	v_bfe_u32 v172, v50, 3, 7
	s_and_b32 s13, s6, s70
	s_lshl_b64 s[6:7], s[8:9], 13
	v_or_b32_e32 v0, v4, v172
	s_or_b32 s6, s6, s13
	v_lshlrev_b32_e32 v51, 3, v49
	v_lshlrev_b32_e32 v64, s12, v0
	v_and_b32_e32 v48, 56, v51
	v_lshl_add_u64 v[0:1], s[6:7], 0, v[64:65]
	v_lshlrev_b64 v[0:1], 7, v[0:1]
	v_lshlrev_b32_e32 v5, 1, v48
	v_or_b32_e32 v0, v0, v5
	v_add_u32_e32 v52, 0x200, v50
	v_lshl_add_u64 v[2:3], s[76:77], 0, v[0:1]
	v_lshl_add_u64 v[0:1], s[78:79], 0, v[0:1]
	v_bfe_u32 v174, v52, 3, 7
	s_barrier
	global_load_dwordx4 v[16:19], v[2:3], off
	global_load_dwordx4 v[20:23], v[0:1], off
	v_or_b32_e32 v0, v4, v174
	v_lshlrev_b32_e32 v64, s12, v0
	v_lshl_add_u64 v[0:1], s[6:7], 0, v[64:65]
	v_lshlrev_b64 v[0:1], 7, v[0:1]
	v_or_b32_e32 v0, v0, v5
	v_lshl_add_u64 v[2:3], s[76:77], 0, v[0:1]
	v_lshl_add_u64 v[0:1], s[78:79], 0, v[0:1]
	s_lshl_b32 s14, s25, 7
	global_load_dwordx4 v[24:27], v[2:3], off
	global_load_dwordx4 v[28:31], v[0:1], off
	v_or_b32_e32 v0, s14, v172
	v_lshlrev_b32_e32 v64, s12, v0
	v_lshl_add_u64 v[0:1], s[6:7], 0, v[64:65]
	v_lshlrev_b64 v[0:1], 7, v[0:1]
	v_or_b32_e32 v0, v0, v5
	v_add_u32_e32 v53, 0x600, v50
	v_lshl_add_u64 v[2:3], s[76:77], 0, v[0:1]
	v_lshl_add_u64 v[0:1], s[78:79], 0, v[0:1]
	v_bfe_u32 v175, v53, 3, 7
	global_load_dwordx4 v[32:35], v[2:3], off
	global_load_dwordx4 v[36:39], v[0:1], off
	v_or_b32_e32 v0, s14, v175
	v_lshlrev_b32_e32 v64, s12, v0
	v_lshl_add_u64 v[0:1], s[6:7], 0, v[64:65]
	v_lshlrev_b64 v[0:1], 7, v[0:1]
	v_or_b32_e32 v0, v0, v5
	v_bfe_u32 v56, v49, 4, 2
	v_lshl_add_u64 v[2:3], s[76:77], 0, v[0:1]
	v_lshl_add_u64 v[0:1], s[78:79], 0, v[0:1]
	v_and_b32_e32 v55, 15, v49
	v_lshlrev_b32_e32 v57, 2, v56
	global_load_dwordx4 v[40:43], v[2:3], off
	global_load_dwordx4 v[44:47], v[0:1], off
	v_cmp_lt_u32_e32 vcc, v57, v55
	v_mov_b32_e32 v8, 0xfe967699
	v_cmp_gt_u32_e64 s[6:7], v57, v55
	v_or_b32_e32 v1, 1, v57
	v_or_b32_e32 v2, 2, v57
	v_cndmask_b32_e32 v4, 0, v8, vcc
	v_cndmask_b32_e64 v0, 0, v8, s[6:7]
	v_cmp_lt_u32_e64 s[6:7], v1, v55
	v_cndmask_b32_e64 v1, v8, 0, vcc
	v_cmp_lt_u32_e32 vcc, v2, v55
	v_or_b32_e32 v3, 3, v57
	s_ashr_i32 s11, s10, 31
	v_cndmask_b32_e32 v6, 0, v8, vcc
	v_cmp_gt_u32_e32 vcc, v2, v55
	v_cndmask_b32_e64 v5, 0, v8, s[6:7]
	s_lshl_b64 s[6:7], s[10:11], 13
	v_cndmask_b32_e32 v2, 0, v8, vcc
	v_cmp_lt_u32_e32 vcc, v3, v55
	s_lshl_b32 s10, s23, 4
	s_add_i32 s14, s14, s10
	v_cndmask_b32_e32 v7, 0, v8, vcc
	v_cmp_gt_u32_e32 vcc, v3, v55
	s_or_b32 s6, s6, s13
	v_and_b32_e32 v160, 48, v49
	v_lshrrev_b32_e32 v204, 2, v55
	v_lshrrev_b32_e32 v205, 3, v55
	v_xor_b32_e32 v204, v204, v205
	v_and_b32_e32 v204, 1, v204
	v_lshlrev_b32_e32 v204, 4, v204
	v_xor_b32_e32 v215, v160, v204
	v_cndmask_b32_e32 v3, 0, v8, vcc
	v_or_b32_e32 v8, s14, v55
	v_ashrrev_i32_e32 v9, 31, v8
	v_lshlrev_b64 v[8:9], s12, v[8:9]
	v_lshl_add_u64 v[166:167], s[6:7], 0, v[8:9]
	s_lshl_b64 s[6:7], s[8:9], 20
	s_add_u32 s6, s64, s6
	v_lshlrev_b32_e32 v8, 7, v166
	s_addc_u32 s7, s65, s7
	v_and_b32_e32 v64, 0xfff80, v8
	v_lshl_add_u64 v[8:9], s[6:7], 0, v[64:65]
	v_mov_b32_e32 v161, v65
	v_lshl_add_u64 v[12:13], v[8:9], 0, v[160:161]
	global_load_dwordx4 v[8:11], v[12:13], off
	s_nop 0
	global_load_dwordx4 v[12:15], v[12:13], off offset:64
	v_lshrrev_b32_e32 v58, 3, v50
	v_add_u32_e32 v59, 0x400, v50
	v_lshlrev_b32_e32 v50, 3, v56
	v_lshlrev_b32_e32 v56, 4, v49
	s_movk_i32 s26, 0x90
	v_lshrrev_b32_e32 v52, 3, v52
	v_and_b32_e32 v176, 0x70, v56
	v_lshrrev_b32_e32 v204, 2, v58
	v_lshrrev_b32_e32 v205, 3, v58
	v_xor_b32_e32 v204, v204, v205
	v_and_b32_e32 v204, 1, v204
	v_lshlrev_b32_e32 v204, 4, v204
	v_xor_b32_e32 v176, v176, v204
	v_and_b32_e32 v216, 1, v58
	v_lshlrev_b32_e32 v216, 4, v216
	v_mul_lo_u32 v177, v58, s26
	v_add3_u32 v56, 0, v177, v176
	v_mul_lo_u32 v178, v52, s26
	s_waitcnt vmcnt(0)
	ds_write_b128 v56, v[16:19]
	v_sub_u32_e32 v217, v56, v216
	ds_write_b128 v217, v[20:23] offset:36864
	v_add3_u32 v16, 0, v178, v176
	s_add_i32 s6, s10, 16
	ds_write_b128 v16, v[24:27]
	v_sub_u32_e32 v217, v16, v216
	ds_write_b128 v217, v[28:31] offset:36864
	v_lshrrev_b32_e32 v16, 3, v59
	v_or_b32_e32 v17, s6, v55
	s_add_i32 s6, s10, 32
	v_lshrrev_b32_e32 v53, 3, v53
	v_mul_lo_u32 v179, v16, s26
	v_mul_lo_u32 v183, v17, s26
	v_or_b32_e32 v17, s6, v55
	s_add_i32 s6, s10, 48
	v_add3_u32 v16, 0, v179, v176
	v_mul_lo_u32 v180, v53, s26
	v_mul_lo_u32 v184, v17, s26
	v_or_b32_e32 v17, s6, v55
	s_add_i32 s6, s10, 64
	ds_write_b128 v16, v[32:35]
	v_sub_u32_e32 v217, v16, v216
	ds_write_b128 v217, v[36:39] offset:36864
	v_add3_u32 v16, 0, v180, v176
	v_mul_lo_u32 v185, v17, s26
	v_or_b32_e32 v17, s6, v55
	s_add_i32 s6, s10, 0x50
	ds_write_b128 v16, v[40:43]
	v_sub_u32_e32 v217, v16, v216
	ds_write_b128 v217, v[44:47] offset:36864
	v_bfe_u32 v16, v49, 2, 2
	v_mul_lo_u32 v186, v17, s26
	v_or_b32_e32 v17, s6, v55
	s_add_i32 s6, s10, 0x60
	s_and_b32 s22, s8, 15
	v_or_b32_e32 v181, s10, v55
	v_or3_b32 v16, v16, s10, v57
	v_mul_lo_u32 v187, v17, s26
	v_or_b32_e32 v17, s6, v55
	s_add_i32 s6, s10, 0x70
	s_addk_i32 s10, 0x80
	s_cmp_lt_i32 s23, 8
	s_cselect_b64 s[20:21], -1, 0
	s_cmp_lt_i32 s23, 7
	s_cselect_b64 s[18:19], -1, 0
	s_cmp_lt_i32 s23, 6
	s_cselect_b64 s[16:17], -1, 0
	s_cmp_lt_i32 s23, 5
	s_cselect_b64 s[14:15], -1, 0
	s_cmp_lt_i32 s23, 4
	v_mul_lo_u32 v188, v17, s26
	v_or_b32_e32 v17, s6, v55
	s_cselect_b64 s[12:13], -1, 0
	s_cmp_lt_i32 s23, 3
	v_mul_lo_u32 v189, v17, s26
	v_or_b32_e32 v17, s10, v55
	s_cselect_b64 s[10:11], -1, 0
	s_cmp_lt_i32 s23, 2
	v_and_b32_e32 v54, 63, v49
	s_cselect_b64 s[8:9], -1, 0
	s_cmp_lt_i32 s23, 1
	s_mov_b32 s71, s63
	s_mov_b32 s38, 0
	v_and_b32_e32 v171, 24, v51
	v_lshrrev_b32_e32 v204, 4, v49
	v_lshrrev_b32_e32 v205, 5, v49
	v_xor_b32_e32 v204, v204, v205
	v_and_b32_e32 v204, 1, v204
	v_lshlrev_b32_e32 v204, 4, v204
	v_xor_b32_e32 v171, v171, v204
	v_bfe_u32 v204, v49, 2, 1
	v_lshlrev_b32_e32 v204, 4, v204
	v_sub_u32_e32 v171, v171, v204
	v_cmp_gt_u32_e32 vcc, 16, v54
	v_mul_lo_u32 v182, v181, s26
	v_mul_lo_u32 v190, v17, s26
	s_cselect_b64 s[6:7], -1, 0
	v_mul_lo_u32 v173, v16, s26
	s_or_b32 s39, s24, 32
	v_lshlrev_b32_e32 v191, 1, v48
	v_lshlrev_b32_e32 v168, 1, v50
	s_waitcnt lgkmcnt(0)
	s_barrier

.LBB0_416:
	s_or_b64 exec, exec, s[36:37]
	s_add_i32 s38, s38, 1
	s_and_b32 s22, s34, 15
	s_xor_b32 s23, s49, 1
	s_mul_i32 s23, s23, 0x12000
	s_add_i32 s23, s23, 0
	v_add3_u32 v48, s23, v177, v176
	s_waitcnt vmcnt(10)
	ds_write_b128 v48, v[16:19]
	s_waitcnt vmcnt(9)
	v_sub_u32_e32 v217, v48, v216
	ds_write_b128 v217, v[20:23] offset:36864
	v_add3_u32 v16, s23, v178, v176
	s_waitcnt vmcnt(8)
	ds_write_b128 v16, v[24:27]
	s_waitcnt vmcnt(7)
	v_sub_u32_e32 v217, v16, v216
	ds_write_b128 v217, v[28:31] offset:36864
	v_add3_u32 v16, s23, v179, v176
	s_add_i32 s39, s39, 32
	s_waitcnt vmcnt(6)
	ds_write_b128 v16, v[32:35]
	s_waitcnt vmcnt(5)
	v_sub_u32_e32 v217, v16, v216
	ds_write_b128 v217, v[36:39] offset:36864
	v_add3_u32 v16, s23, v180, v176
	s_cmpk_eq_i32 s38, 0x5f
	s_waitcnt vmcnt(4)
	ds_write_b128 v16, v[40:43]
	s_waitcnt vmcnt(3)
	v_sub_u32_e32 v217, v16, v216
	ds_write_b128 v217, v[44:47] offset:36864
	s_waitcnt lgkmcnt(0)
	s_barrier
	s_cbranch_scc1 .LBB0_418
	s_mov_b32 s30, s24
	v_mov_b64_e32 v[166:167], v[164:165]
	s_branch .LBB0_412
